# GEMM prologues: the wr==1 stagger barrier also moved below K-tile 1's loads (7 of 12 sites)
# speedup vs baseline: 1.0085x; 1.0085x over previous
.LBB0_1011:
	s_andn2_b64 vcc, exec, s[0:1]
	v_writelane_b32 v255, s51, 18
	s_cbranch_vccnz .LBB0_1275
	v_mbcnt_lo_u32_b32 v0, -1, 0
	v_mbcnt_hi_u32_b32 v0, -1, v0
	v_readlane_b32 s0, v254, 2
	v_add_u32_e32 v0, s79, v0
	v_readlane_b32 s1, v254, 3
	s_load_dword s56, s[0:1], 0x0
	s_mov_b32 s57, s96
	s_mov_b32 s0, 24
	s_waitcnt lgkmcnt(0)
	s_ashr_i32 s1, s0, 31
	s_lshl_b64 s[0:1], s[0:1], 3
	s_add_u32 s0, s92, s0
	s_addc_u32 s1, s93, s1
	s_load_dwordx2 s[28:29], s[0:1], 0x0
	v_writelane_b32 v255, s38, 19
	s_mul_i32 s0, s51, 0x2200000
	s_mov_b32 s5, s91
	v_writelane_b32 v255, s39, 20
	s_waitcnt lgkmcnt(0)
	s_add_u32 s74, s28, 0x600000
	s_addc_u32 s75, s29, 0
	s_add_u32 s58, s28, 0x58000000
	s_addc_u32 s59, s29, 0
	s_add_u32 s0, s28, s0
	v_writelane_b32 v255, s40, 21
	s_addc_u32 s1, s29, 0
	s_add_u32 s0, s0, 0xa00000
	v_writelane_b32 v255, s41, 22
	v_writelane_b32 v255, s0, 23
	s_addc_u32 s0, s1, 0
	v_writelane_b32 v255, s0, 24
	v_writelane_b32 v255, s28, 25
	s_cmpk_gt_i32 s57, 0x5ff
	v_mbcnt_lo_u32_b32 v0, -1, 0
	v_mbcnt_hi_u32_b32 v0, -1, v0
	s_nop 0
	v_writelane_b32 v255, s29, 26
	s_cbranch_scc1 .LBB0_1036
	v_readlane_b32 s0, v255, 23
	s_add_u32 s33, s0, 0xa00000
	v_readlane_b32 s0, v255, 24
	s_addc_u32 s61, s0, 0
	s_lshl_b32 s66, s5, 6
	v_add_u32_e32 v1, s66, v0
	v_ashrrev_i32_e32 v3, 31, v1
	v_lshrrev_b32_e32 v3, 26, v3
	v_lshlrev_b32_e32 v2, 4, v1
	v_add_u32_e32 v3, v1, v3
	v_bfe_i32 v1, v1, 27, 1
	v_lshrrev_b32_e32 v1, 22, v1
	v_add_u32_e32 v1, v2, v1
	v_and_b32_e32 v1, 0xfffffc00, v1
	v_sub_u32_e32 v1, v2, v1
	v_lshrrev_b32_e32 v4, 4, v1
	v_bitop3_b32 v1, v4, v1, 32 bitop3:0x6c
	v_ashrrev_i32_e32 v5, 31, v1
	v_ashrrev_i32_e32 v3, 6, v3
	v_lshrrev_b32_e32 v5, 26, v5
	v_lshlrev_b32_e32 v4, 3, v3
	v_add_u32_e32 v5, v1, v5
	v_and_b32_e32 v4, -16, v4
	v_ashrrev_i32_e32 v6, 6, v5
	v_and_b32_e32 v5, 0xc0, v5
	v_add_u32_e32 v4, v6, v4
	v_sub_u32_e32 v1, v1, v5
	v_lshlrev_b32_e32 v3, 5, v3
	v_ashrrev_i16_sdwa v1, v231, sext(v1) dst_sel:DWORD dst_unused:UNUSED_PAD src0_sel:DWORD src1_sel:BYTE_0
	v_lshlrev_b32_e32 v5, 1, v4
	v_lshrrev_b32_e32 v7, 2, v4
	v_and_b32_e32 v6, 3, v6
	s_mov_b32 s0, 0x1fffe0
	v_and_b32_e32 v3, 32, v3
	v_bfe_i32 v1, v1, 0, 16
	v_and_b32_e32 v5, 24, v5
	v_and_b32_e32 v7, 4, v7
	v_and_or_b32 v4, v4, s0, v6
	v_or3_b32 v4, v4, v7, v5
	v_add_lshl_u32 v1, v3, v1, 1
	v_lshl_add_u32 v245, v4, 11, v1
	v_add_u32_e32 v1, 0x2000, v2
	v_ashrrev_i32_e32 v2, 31, v1
	v_lshrrev_b32_e32 v2, 22, v2
	v_add_u32_e32 v2, v1, v2
	v_ashrrev_i32_e32 v2, 10, v2
	v_mul_i32_i24_e32 v3, 0x400, v2
	v_sub_u32_e32 v1, v1, v3
	v_lshrrev_b32_e32 v3, 4, v1
	v_bitop3_b32 v1, v3, v1, 32 bitop3:0x6c
	v_ashrrev_i32_e32 v4, 31, v1
	v_lshrrev_b32_e32 v4, 26, v4
	v_lshlrev_b32_e32 v3, 3, v2
	v_add_u32_e32 v4, v1, v4
	v_and_b32_e32 v3, -16, v3
	v_ashrrev_i32_e32 v5, 6, v4
	v_and_b32_e32 v4, 0xc0, v4
	v_add_u32_e32 v3, v5, v3
	v_sub_u32_e32 v1, v1, v4
	v_lshlrev_b32_e32 v2, 5, v2
	v_ashrrev_i16_sdwa v1, v231, sext(v1) dst_sel:DWORD dst_unused:UNUSED_PAD src0_sel:DWORD src1_sel:BYTE_0
	v_lshlrev_b32_e32 v4, 1, v3
	v_lshrrev_b32_e32 v6, 2, v3
	v_and_b32_e32 v5, 3, v5
	s_ashr_i32 s67, s57, 31
	v_and_b32_e32 v2, 32, v2
	v_bfe_i32 v1, v1, 0, 16
	v_and_b32_e32 v4, 24, v4
	v_and_b32_e32 v6, 4, v6
	v_and_or_b32 v3, v3, s0, v5
	s_lshr_b32 s0, s67, 29
	v_or3_b32 v3, v3, v6, v4
	v_add_lshl_u32 v1, v2, v1, 1
	s_add_i32 s0, s57, s0
	v_lshl_add_u32 v244, v3, 11, v1
	s_ashr_i32 s1, s0, 3
	s_and_b32 s0, s0, -8
	v_mov_b32 v12, 0
	v_mbcnt_lo_u32_b32 v1, -1, 0
	v_mbcnt_hi_u32_b32 v1, -1, v1
	s_ashr_i32 s12, s5, 2
	s_lshl_b32 s8, s5, 10
	s_sub_i32 s0, s57, s0
	v_add_u32_e32 v1, s66, v1
	s_cmp_lt_i32 s0, 0
	s_movk_i32 s2, 0xc1
	v_ashrrev_i32_e32 v3, 31, v1
	s_cselect_b32 s2, s2, 0xc0
	v_lshrrev_b32_e32 v3, 26, v3
	s_mul_i32 s0, s0, s2
	v_lshlrev_b32_e32 v2, 4, v1
	v_add_u32_e32 v3, v1, v3
	v_bfe_i32 v1, v1, 27, 1
	s_add_i32 s0, s0, s1
	v_lshrrev_b32_e32 v1, 22, v1
	s_mul_hi_i32 s1, s0, 0x2aaaaaab
	v_add_u32_e32 v1, v2, v1
	s_lshr_b32 s2, s1, 31
	s_ashr_i32 s1, s1, 5
	v_and_b32_e32 v1, 0xfffffc00, v1
	s_add_i32 s1, s1, s2
	v_sub_u32_e32 v1, v2, v1
	s_mul_i32 s2, s1, 0xc0
	v_lshrrev_b32_e32 v4, 4, v1
	s_sub_i32 s0, s0, s2
	v_bitop3_b32 v1, v4, v1, 32 bitop3:0x6c
	s_bfe_u32 s2, s0, 0x3001c
	v_ashrrev_i32_e32 v5, 31, v1
	s_add_i32 s2, s0, s2
	v_lshrrev_b32_e32 v5, 26, v5
	s_sext_i32_i16 s3, s2
	s_and_b32 s2, s2, 0xfff8
	v_add_u32_e32 v5, v1, v5
	s_sub_i32 s0, s0, s2
	v_lshrrev_b32_e32 v6, 6, v5
	v_and_b32_e32 v5, 0xc0, v5
	v_add_u32_e32 v2, 0x2000, v2
	s_lshl_b32 s1, s1, 3
	s_sext_i32_i16 s0, s0
	v_sub_u32_e32 v1, v1, v5
	v_ashrrev_i32_e32 v5, 31, v2
	s_add_i32 s0, s1, s0
	v_ashrrev_i32_e32 v3, 6, v3
	v_lshrrev_b32_e32 v5, 22, v5
	s_ashr_i32 s1, s0, 31
	v_lshlrev_b32_e32 v4, 3, v3
	v_add_u32_e32 v5, v2, v5
	s_lshr_b32 s4, s3, 3
	s_lshl_b64 s[2:3], s[0:1], 19
	v_and_b32_e32 v4, 0x1ffff0, v4
	v_ashrrev_i32_e32 v5, 10, v5
	s_add_u32 s40, s58, s2
	v_add_u32_e32 v4, v6, v4
	v_mul_i32_i24_e32 v6, 0x400, v5
	s_addc_u32 s1, s59, s3
	s_bfe_i64 s[2:3], s[4:5], 0x100000
	v_sub_u32_e32 v2, v2, v6
	s_lshl_b64 s[2:3], s[2:3], 19
	v_lshrrev_b32_e32 v6, 4, v2
	s_add_u32 s52, s33, s2
	v_bitop3_b32 v2, v6, v2, 32 bitop3:0x6c
	s_addc_u32 s2, s61, s3
	v_ashrrev_i32_e32 v7, 31, v2
	s_add_i32 s68, s8, 0
	v_lshrrev_b32_e32 v7, 26, v7
	s_add_i32 s69, s68, 0x10000
	s_and_b32 s53, s2, 0xffff
	v_add_u32_e32 v7, v2, v7
	s_mov_b32 m0, s69
	s_add_i32 s70, s68, 0x12000
	v_lshlrev_b32_e32 v3, 5, v3
	v_lshlrev_b32_e32 v6, 3, v5
	s_waitcnt vmcnt(0)
	v_lshrrev_b32_e32 v8, 6, v7
	v_and_b32_e32 v7, 0xc0, v7
	buffer_load_dwordx4 v245, s[52:55], 0 offen lds
	s_mov_b32 m0, s70
	s_add_i32 s71, s68, 0x14000
	v_and_b32_e32 v3, 32, v3
	v_ashrrev_i16_sdwa v1, v231, sext(v1) dst_sel:DWORD dst_unused:UNUSED_PAD src0_sel:DWORD src1_sel:BYTE_0
	v_and_b32_e32 v6, 0x1ffff0, v6
	v_lshlrev_b32_e32 v5, 5, v5
	v_sub_u32_e32 v2, v2, v7
	buffer_load_dwordx4 v244, s[52:55], 0 offen lds
	s_mov_b32 m0, s71
	s_add_i32 s72, s68, 0x16000
	v_bfe_i32 v1, v1, 0, 16
	v_add_u32_e32 v6, v8, v6
	v_and_b32_e32 v5, 32, v5
	v_ashrrev_i16_sdwa v2, v231, sext(v2) dst_sel:DWORD dst_unused:UNUSED_PAD src0_sel:DWORD src1_sel:BYTE_0
	v_lshl_or_b32 v3, v4, 10, v3
	buffer_load_dwordx4 v245, s[52:55], s89 offen lds
	s_mov_b32 m0, s72
	v_bfe_i32 v2, v2, 0, 16
	v_lshl_or_b32 v4, v6, 10, v5
	v_add_lshl_u32 v132, v3, v1, 1
	buffer_load_dwordx4 v244, s[52:55], s89 offen lds
	s_and_b32 s41, s1, 0xffff
	s_mov_b32 s42, s54
	s_mov_b32 s43, s55
	s_mov_b32 m0, s68
	s_add_i32 s73, s68, 0x2000
	v_add_lshl_u32 v133, v4, v2, 1
	buffer_load_dwordx4 v132, s[40:43], 0 offen lds
	s_mov_b32 m0, s73
	s_add_i32 s76, s68, 0x4000
	buffer_load_dwordx4 v133, s[40:43], 0 offen lds
	s_mov_b32 m0, s76
	s_add_i32 s77, s68, 0x6000
	buffer_load_dwordx4 v132, s[40:43], s89 offen lds
	s_mov_b32 m0, s77
	s_cmp_eq_u32 s12, 1
	buffer_load_dwordx4 v133, s[40:43], s89 offen lds
	s_cselect_b64 s[2:3], -1, 0
	s_add_u32 s8, s28, 0x38000000
	s_addc_u32 s9, s29, 0
	s_add_i32 s78, s68, 0x18000
	s_mov_b32 m0, s78
	s_movk_i32 s1, 0x80
	s_add_i32 s79, s68, 0x1a000
	buffer_load_dwordx4 v245, s[52:55], s1 offen lds
	s_mov_b32 m0, s79
	s_add_i32 s80, s68, 0x8000
	buffer_load_dwordx4 v244, s[52:55], s1 offen lds
	s_mov_b32 s42, s54
	s_mov_b32 s43, s55
	s_mov_b32 m0, s80
	s_add_i32 s82, s68, 0xa000
	buffer_load_dwordx4 v132, s[40:43], s1 offen lds
	s_mov_b32 m0, s82
	s_add_i32 s83, s68, 0x1c000
	buffer_load_dwordx4 v133, s[40:43], s1 offen lds
	s_mov_b32 m0, s83
	s_mov_b32 s1, 0x40080
	s_add_i32 s88, s68, 0x1e000
	buffer_load_dwordx4 v245, s[52:55], s1 offen lds
	s_mov_b32 m0, s88
	s_sext_i32_i16 s95, s4
	buffer_load_dwordx4 v244, s[52:55], s1 offen lds
	s_cmp_lg_u32 s12, 1
	s_cbranch_scc1 .LBB0_1015
	s_barrier
.LBB0_1015:
	s_waitcnt vmcnt(8)
	s_barrier
	v_and_b32_e32 v1, 48, v0
	v_lshlrev_b32_e32 v2, 6, v0
	s_movk_i32 s4, 0x3c0
	v_lshlrev_b32_e32 v0, 2, v0
	s_lshl_b32 s1, s12, 13
	v_and_or_b32 v1, v2, s4, v1
	v_and_b32_e32 v0, 32, v0
	v_bitop3_b32 v2, v1, s1, v0 bitop3:0xde
	s_lshl_b32 s1, s5, 5
	s_and_b32 s90, s1, 0x60
	s_lshl_b32 s1, s90, 7
	s_lshl_b32 s89, s12, 6
	v_bitop3_b32 v0, v1, s1, v0 bitop3:0xde
	s_waitcnt vmcnt(6)
	s_add_i32 s91, s68, 0xc000
	s_cmp_lt_u32 s5, 4
	v_add_u32_e32 v0, 0, v0
	v_mov_b32_e32 v13, v12
	v_mov_b32_e32 v14, v12
	v_mov_b32_e32 v15, v12
	s_cselect_b64 s[18:19], -1, 0
	s_add_i32 s92, s68, 0xe000
	s_ashr_i32 s93, s56, 31
	s_mov_b32 s94, 0
	s_mov_b64 s[64:65], -1
	v_add_u32_e32 v134, 0x10000, v0
	v_add_u32_e32 v135, 0x14000, v0
	v_add_u32_e32 v136, 0, v2
	v_add_u32_e32 v137, 0x18000, v0
	v_add_u32_e32 v138, 0x1c000, v0
	s_mov_b64 s[42:43], s[54:55]
	s_mov_b64 s[4:5], s[54:55]
	s_barrier
	s_branch .LBB0_1018

.LBB0_1171:
	s_lshl_b32 s65, s5, 6
	v_add_u32_e32 v0, s65, v4
	v_ashrrev_i32_e32 v2, 31, v0
	v_lshrrev_b32_e32 v2, 26, v2
	v_lshlrev_b32_e32 v1, 4, v0
	v_add_u32_e32 v2, v0, v2
	v_bfe_i32 v0, v0, 27, 1
	v_lshrrev_b32_e32 v0, 22, v0
	v_add_u32_e32 v0, v1, v0
	v_and_b32_e32 v0, 0xfffffc00, v0
	v_sub_u32_e32 v0, v1, v0
	v_lshrrev_b32_e32 v3, 4, v0
	v_bitop3_b32 v0, v3, v0, 32 bitop3:0x6c
	v_ashrrev_i32_e32 v5, 31, v0
	v_ashrrev_i32_e32 v2, 6, v2
	v_lshrrev_b32_e32 v5, 26, v5
	v_lshlrev_b32_e32 v3, 3, v2
	v_add_u32_e32 v5, v0, v5
	v_and_b32_e32 v3, -16, v3
	v_ashrrev_i32_e32 v6, 6, v5
	v_and_b32_e32 v5, 0xc0, v5
	v_add_u32_e32 v3, v6, v3
	v_sub_u32_e32 v0, v0, v5
	v_lshlrev_b32_e32 v2, 5, v2
	v_ashrrev_i16_sdwa v0, v231, sext(v0) dst_sel:DWORD dst_unused:UNUSED_PAD src0_sel:DWORD src1_sel:BYTE_0
	v_lshlrev_b32_e32 v5, 1, v3
	v_lshrrev_b32_e32 v7, 2, v3
	v_and_b32_e32 v6, 3, v6
	s_mov_b32 s1, 0x1fffe0
	v_and_b32_e32 v2, 32, v2
	v_bfe_i32 v0, v0, 0, 16
	v_and_b32_e32 v5, 24, v5
	v_and_b32_e32 v7, 4, v7
	v_and_or_b32 v3, v3, s1, v6
	v_or3_b32 v3, v3, v7, v5
	v_add_lshl_u32 v0, v2, v0, 1
	v_lshl_add_u32 v144, v3, 11, v0
	v_add_u32_e32 v0, 0x2000, v1
	v_ashrrev_i32_e32 v1, 31, v0
	v_lshrrev_b32_e32 v1, 22, v1
	v_add_u32_e32 v1, v0, v1
	v_ashrrev_i32_e32 v1, 10, v1
	v_mul_i32_i24_e32 v2, 0x400, v1
	v_sub_u32_e32 v0, v0, v2
	v_lshrrev_b32_e32 v2, 4, v0
	v_bitop3_b32 v0, v2, v0, 32 bitop3:0x6c
	v_ashrrev_i32_e32 v3, 31, v0
	v_lshrrev_b32_e32 v3, 26, v3
	v_lshlrev_b32_e32 v2, 3, v1
	v_add_u32_e32 v3, v0, v3
	v_and_b32_e32 v2, -16, v2
	v_ashrrev_i32_e32 v5, 6, v3
	v_add_u32_e32 v2, v5, v2
	v_and_b32_e32 v3, 0xc0, v3
	v_and_b32_e32 v5, 3, v5
	s_add_i32 s0, s2, s0
	v_sub_u32_e32 v0, v0, v3
	v_lshlrev_b32_e32 v3, 1, v2
	v_lshrrev_b32_e32 v6, 2, v2
	v_and_or_b32 v2, v2, s1, v5
	s_ashr_i32 s1, s0, 31
	s_lshr_b32 s1, s1, 23
	s_add_i32 s1, s0, s1
	s_ashr_i32 s2, s1, 9
	s_and_b32 s1, s1, 0xfffffe00
	s_lshl_b32 s2, s2, 3
	v_lshlrev_b32_e32 v1, 5, v1
	v_ashrrev_i16_sdwa v0, v231, sext(v0) dst_sel:DWORD dst_unused:UNUSED_PAD src0_sel:DWORD src1_sel:BYTE_0
	s_sub_i32 s3, s0, s1
	s_sub_i32 s0, 4, s2
	v_and_b32_e32 v1, 32, v1
	v_bfe_i32 v0, v0, 0, 16
	v_and_b32_e32 v3, 24, v3
	v_and_b32_e32 v6, 4, v6
	s_min_u32 s8, s0, 8
	v_or3_b32 v2, v2, v6, v3
	v_add_lshl_u32 v0, v1, v0, 1
	v_cvt_f32_ubyte0_e32 v1, s8
	v_lshl_add_u32 v145, v2, 11, v0
	v_cvt_f32_i32_e32 v0, s3
	v_rcp_iflag_f32_e32 v2, v1
	s_ashr_i32 s0, s3, 30
	s_or_b32 s4, s0, 1
	s_ashr_i32 s12, s5, 2
	v_mul_f32_e32 v2, v0, v2
	v_trunc_f32_e32 v2, v2
	v_fma_f32 v0, -v2, v1, v0
	v_cvt_i32_f32_e32 v2, v2
	v_cmp_ge_f32_e64 s[0:1], |v0|, v1
	v_mov_b32 v0, 0
	v_mbcnt_lo_u32_b32 v1, -1, 0
	v_mbcnt_hi_u32_b32 v1, -1, v1
	s_lshl_b32 s9, s5, 10
	v_add_u32_e32 v1, s65, v1
	v_ashrrev_i32_e32 v3, 31, v1
	s_and_b64 s[0:1], s[0:1], exec
	v_lshrrev_b32_e32 v3, 26, v3
	v_readfirstlane_b32 s1, v2
	v_lshlrev_b32_e32 v2, 4, v1
	v_add_u32_e32 v3, v1, v3
	v_bfe_i32 v1, v1, 27, 1
	v_lshrrev_b32_e32 v1, 22, v1
	v_add_u32_e32 v1, v2, v1
	v_and_b32_e32 v1, 0xfffffc00, v1
	v_sub_u32_e32 v1, v2, v1
	v_lshrrev_b32_e32 v5, 4, v1
	v_bitop3_b32 v1, v5, v1, 32 bitop3:0x6c
	s_cselect_b32 s0, s4, 0
	v_ashrrev_i32_e32 v6, 31, v1
	s_add_i32 s4, s1, s0
	v_lshrrev_b32_e32 v6, 26, v6
	s_mul_i32 s0, s4, s8
	v_add_u32_e32 v6, v1, v6
	s_sub_i32 s0, s3, s0
	v_lshrrev_b32_e32 v7, 6, v6
	v_and_b32_e32 v6, 0xc0, v6
	v_add_u32_e32 v2, 0x2000, v2
	s_sext_i32_i16 s0, s0
	v_sub_u32_e32 v1, v1, v6
	v_ashrrev_i32_e32 v6, 31, v2
	s_add_i32 s62, s2, s0
	v_ashrrev_i32_e32 v3, 6, v3
	v_lshrrev_b32_e32 v6, 22, v6
	s_ashr_i32 s63, s62, 31
	v_lshlrev_b32_e32 v5, 3, v3
	v_add_u32_e32 v6, v2, v6
	s_lshl_b64 s[0:1], s[62:63], 19
	v_and_b32_e32 v5, 0x1ffff0, v5
	v_ashrrev_i32_e32 v6, 10, v6
	s_add_u32 s40, s33, s0
	v_add_u32_e32 v5, v7, v5
	v_mul_i32_i24_e32 v7, 0x400, v6
	s_addc_u32 s2, s61, s1
	s_bfe_i64 s[0:1], s[4:5], 0x100000
	v_sub_u32_e32 v2, v2, v7
	s_lshl_b64 s[0:1], s[0:1], 19
	v_lshrrev_b32_e32 v7, 4, v2
	s_add_u32 s52, s58, s0
	v_bitop3_b32 v2, v7, v2, 32 bitop3:0x6c
	s_addc_u32 s0, s59, s1
	s_waitcnt vmcnt(0)
	v_ashrrev_i32_e32 v8, 31, v2
	s_add_i32 s63, s9, 0
	v_lshrrev_b32_e32 v8, 26, v8
	s_add_i32 s66, s63, 0x10000
	s_and_b32 s53, s0, 0xffff
	v_add_u32_e32 v8, v2, v8
	s_mov_b32 m0, s66
	s_add_i32 s67, s63, 0x12000
	v_lshlrev_b32_e32 v3, 5, v3
	v_lshlrev_b32_e32 v7, 3, v6
	v_lshrrev_b32_e32 v9, 6, v8
	v_and_b32_e32 v8, 0xc0, v8
	buffer_load_dwordx4 v144, s[52:55], 0 offen lds
	s_mov_b32 m0, s67
	s_add_i32 s68, s63, 0x14000
	v_and_b32_e32 v3, 32, v3
	v_ashrrev_i16_sdwa v1, v231, sext(v1) dst_sel:DWORD dst_unused:UNUSED_PAD src0_sel:DWORD src1_sel:BYTE_0
	v_and_b32_e32 v7, 0x1ffff0, v7
	v_lshlrev_b32_e32 v6, 5, v6
	v_sub_u32_e32 v2, v2, v8
	buffer_load_dwordx4 v145, s[52:55], 0 offen lds
	s_mov_b32 m0, s68
	s_add_i32 s69, s63, 0x16000
	v_bfe_i32 v1, v1, 0, 16
	v_add_u32_e32 v7, v9, v7
	v_and_b32_e32 v6, 32, v6
	v_ashrrev_i16_sdwa v2, v231, sext(v2) dst_sel:DWORD dst_unused:UNUSED_PAD src0_sel:DWORD src1_sel:BYTE_0
	v_lshl_or_b32 v3, v5, 10, v3
	buffer_load_dwordx4 v144, s[52:55], s89 offen lds
	s_mov_b32 m0, s69
	v_bfe_i32 v2, v2, 0, 16
	v_lshl_or_b32 v5, v7, 10, v6
	v_add_lshl_u32 v146, v3, v1, 1
	buffer_load_dwordx4 v145, s[52:55], s89 offen lds
	s_and_b32 s41, s2, 0xffff
	s_mov_b32 s42, s54
	s_mov_b32 s43, s55
	s_mov_b32 m0, s63
	s_add_i32 s70, s63, 0x2000
	v_add_lshl_u32 v147, v5, v2, 1
	buffer_load_dwordx4 v146, s[40:43], 0 offen lds
	s_mov_b32 m0, s70
	s_add_i32 s71, s63, 0x4000
	buffer_load_dwordx4 v147, s[40:43], 0 offen lds
	s_mov_b32 m0, s71
	s_add_i32 s72, s63, 0x6000
	buffer_load_dwordx4 v146, s[40:43], s89 offen lds
	s_mov_b32 m0, s72
	s_cmp_eq_u32 s12, 1
	buffer_load_dwordx4 v147, s[40:43], s89 offen lds
	s_cselect_b64 s[0:1], -1, 0
	s_and_b32 s73, s5, 3
	s_lshl_b32 s8, s12, 13
	s_lshl_b32 s9, s73, 12
	s_add_u32 s2, s28, 0x35000000
	s_addc_u32 s3, s29, 0
	s_add_i32 s76, s63, 0x18000
	s_mov_b32 m0, s76
	s_movk_i32 s13, 0x80
	s_add_i32 s77, s63, 0x1a000
	buffer_load_dwordx4 v144, s[52:55], s13 offen lds
	s_mov_b32 m0, s77
	s_add_i32 s78, s63, 0x8000
	buffer_load_dwordx4 v145, s[52:55], s13 offen lds
	s_mov_b32 s42, s54
	s_mov_b32 s43, s55
	s_mov_b32 m0, s78
	s_add_i32 s79, s63, 0xa000
	buffer_load_dwordx4 v146, s[40:43], s13 offen lds
	s_mov_b32 m0, s79
	s_add_i32 s80, s63, 0x1c000
	buffer_load_dwordx4 v147, s[40:43], s13 offen lds
	s_mov_b32 m0, s80
	s_mov_b32 s13, 0x40080
	s_add_i32 s82, s63, 0x1e000
	buffer_load_dwordx4 v144, s[52:55], s13 offen lds
	s_mov_b32 m0, s82
	v_and_b32_e32 v5, 15, v4
	buffer_load_dwordx4 v145, s[52:55], s13 offen lds
	s_cmp_lg_u32 s12, 1
	s_cbranch_scc1 .LBB0_1173
	s_barrier
.LBB0_1173:
	s_waitcnt vmcnt(8)
	s_barrier
	v_and_b32_e32 v6, 48, v4
	v_lshlrev_b32_e32 v4, 2, v4
	s_add_i32 s83, s63, 0xc000
	v_lshl_or_b32 v5, v5, 6, v6
	v_and_b32_e32 v4, 32, v4
	s_cmp_lt_u32 s5, 4
	s_sext_i32_i16 s94, s4
	v_bitop3_b32 v6, v5, s8, v4 bitop3:0xde
	v_bitop3_b32 v4, v5, s9, v4 bitop3:0xde
	s_waitcnt vmcnt(6)
	s_cselect_b64 s[8:9], -1, 0
	s_lshl_b32 s4, s73, 7
	s_add_i32 s88, s4, 0
	v_mov_b32_e32 v1, v0
	v_mov_b32_e32 v2, v0
	v_mov_b32_e32 v3, v0
	s_add_i32 s88, s88, 0x20100
	s_lshl_b32 s89, s12, 8
	s_and_b32 s90, s5, 4
	s_add_i32 s91, s63, 0xe000
	s_ashr_i32 s92, s56, 31
	s_mov_b32 s93, 0
	v_add_u32_e32 v148, 0, v4
	v_add_u32_e32 v149, 0, v6
	s_mov_b64 s[42:43], s[54:55]
	s_mov_b64 s[4:5], s[54:55]
	s_barrier
	s_branch .LBB0_1176

.LBB0_1491:
	s_lshl_b32 s8, s5, 6
	v_add_u32_e32 v1, s8, v0
	v_ashrrev_i32_e32 v3, 31, v1
	v_lshrrev_b32_e32 v3, 26, v3
	v_lshlrev_b32_e32 v2, 4, v1
	v_add_u32_e32 v3, v1, v3
	v_bfe_i32 v1, v1, 27, 1
	v_lshrrev_b32_e32 v1, 22, v1
	v_add_u32_e32 v1, v2, v1
	v_and_b32_e32 v1, 0xfffffc00, v1
	v_sub_u32_e32 v1, v2, v1
	v_lshrrev_b32_e32 v4, 4, v1
	v_bitop3_b32 v1, v4, v1, 32 bitop3:0x6c
	v_ashrrev_i32_e32 v5, 31, v1
	v_ashrrev_i32_e32 v3, 6, v3
	v_lshrrev_b32_e32 v5, 26, v5
	v_lshlrev_b32_e32 v4, 3, v3
	v_add_u32_e32 v5, v1, v5
	v_and_b32_e32 v4, -16, v4
	v_ashrrev_i32_e32 v6, 6, v5
	v_and_b32_e32 v5, 0xc0, v5
	v_add_u32_e32 v4, v6, v4
	v_sub_u32_e32 v1, v1, v5
	v_lshlrev_b32_e32 v3, 5, v3
	v_ashrrev_i16_sdwa v1, v231, sext(v1) dst_sel:DWORD dst_unused:UNUSED_PAD src0_sel:DWORD src1_sel:BYTE_0
	v_lshlrev_b32_e32 v5, 1, v4
	v_lshrrev_b32_e32 v7, 2, v4
	v_and_b32_e32 v6, 3, v6
	s_mov_b32 s3, 0x1fffe0
	v_and_b32_e32 v3, 32, v3
	v_bfe_i32 v1, v1, 0, 16
	v_and_b32_e32 v5, 24, v5
	v_and_b32_e32 v7, 4, v7
	v_and_or_b32 v4, v4, s3, v6
	v_or3_b32 v4, v4, v7, v5
	v_add_lshl_u32 v1, v3, v1, 1
	v_lshl_add_u32 v199, v4, 11, v1
	v_add_u32_e32 v1, 0x2000, v2
	v_ashrrev_i32_e32 v2, 31, v1
	v_lshrrev_b32_e32 v2, 22, v2
	v_add_u32_e32 v2, v1, v2
	v_ashrrev_i32_e32 v2, 10, v2
	v_mul_i32_i24_e32 v3, 0x400, v2
	v_sub_u32_e32 v1, v1, v3
	v_lshrrev_b32_e32 v3, 4, v1
	v_bitop3_b32 v1, v3, v1, 32 bitop3:0x6c
	v_ashrrev_i32_e32 v4, 31, v1
	v_lshrrev_b32_e32 v4, 26, v4
	v_lshlrev_b32_e32 v3, 3, v2
	v_add_u32_e32 v4, v1, v4
	v_and_b32_e32 v3, -16, v3
	v_ashrrev_i32_e32 v5, 6, v4
	v_and_b32_e32 v4, 0xc0, v4
	v_add_u32_e32 v3, v5, v3
	v_sub_u32_e32 v1, v1, v4
	v_lshlrev_b32_e32 v2, 5, v2
	v_ashrrev_i16_sdwa v1, v231, sext(v1) dst_sel:DWORD dst_unused:UNUSED_PAD src0_sel:DWORD src1_sel:BYTE_0
	v_lshlrev_b32_e32 v4, 1, v3
	v_lshrrev_b32_e32 v6, 2, v3
	v_and_b32_e32 v5, 3, v5
	v_and_b32_e32 v2, 32, v2
	v_bfe_i32 v1, v1, 0, 16
	v_and_b32_e32 v4, 24, v4
	v_and_b32_e32 v6, 4, v6
	v_and_or_b32 v3, v3, s3, v5
	v_or3_b32 v3, v3, v6, v4
	v_add_lshl_u32 v1, v2, v1, 1
	v_lshl_add_u32 v228, v3, 11, v1
	s_waitcnt vmcnt(0)
	v_mov_b32 v8, 0
	v_mbcnt_lo_u32_b32 v1, -1, 0
	v_mbcnt_hi_u32_b32 v1, -1, v1
	s_add_i32 s2, s4, s2
	v_add_u32_e32 v1, s8, v1
	v_ashrrev_i32_e32 v3, 31, v1
	v_lshrrev_b32_e32 v3, 26, v3
	v_lshlrev_b32_e32 v2, 4, v1
	v_add_u32_e32 v3, v1, v3
	v_bfe_i32 v1, v1, 27, 1
	s_ashr_i32 s3, s2, 31
	v_lshrrev_b32_e32 v1, 22, v1
	s_lshr_b32 s3, s3, 26
	v_add_u32_e32 v1, v2, v1
	s_add_i32 s3, s2, s3
	v_and_b32_e32 v1, 0xfffffc00, v1
	s_ashr_i32 s4, s3, 6
	s_and_b32 s3, s3, 0xffc0
	v_sub_u32_e32 v1, v2, v1
	s_sub_i32 s2, s2, s3
	v_lshrrev_b32_e32 v4, 4, v1
	s_lshl_b32 s3, s4, 3
	s_bfe_i32 s4, s2, 0x80000
	v_bitop3_b32 v1, v4, v1, 32 bitop3:0x6c
	s_bfe_u32 s4, s4, 0x3000c
	v_ashrrev_i32_e32 v5, 31, v1
	s_add_i32 s13, s2, s4
	v_lshrrev_b32_e32 v5, 26, v5
	s_bfe_i32 s4, s13, 0x80000
	s_and_b32 s13, s13, 0xf8
	v_add_u32_e32 v5, v1, v5
	s_sub_i32 s2, s2, s13
	v_lshrrev_b32_e32 v6, 6, v5
	v_and_b32_e32 v5, 0xc0, v5
	v_add_u32_e32 v2, 0x2000, v2
	s_sext_i32_i8 s2, s2
	v_sub_u32_e32 v1, v1, v5
	v_ashrrev_i32_e32 v5, 31, v2
	s_add_i32 s58, s3, s2
	v_ashrrev_i32_e32 v3, 6, v3
	v_lshrrev_b32_e32 v5, 22, v5
	s_sext_i32_i16 s4, s4
	s_ashr_i32 s59, s58, 31
	v_lshlrev_b32_e32 v4, 3, v3
	v_add_u32_e32 v5, v2, v5
	s_ashr_i32 s12, s5, 2
	s_lshl_b32 s9, s5, 10
	s_lshr_b32 s4, s4, 3
	s_lshl_b64 s[2:3], s[58:59], 19
	v_and_b32_e32 v4, 0x1ffff0, v4
	v_ashrrev_i32_e32 v5, 10, v5
	s_add_u32 s40, s65, s2
	v_add_u32_e32 v4, v6, v4
	v_mul_i32_i24_e32 v6, 0x400, v5
	s_addc_u32 s13, s66, s3
	s_bfe_i64 s[2:3], s[4:5], 0x100000
	v_sub_u32_e32 v2, v2, v6
	s_lshl_b64 s[2:3], s[2:3], 19
	v_lshrrev_b32_e32 v6, 4, v2
	s_add_u32 s52, s67, s2
	v_bitop3_b32 v2, v6, v2, 32 bitop3:0x6c
	s_addc_u32 s2, s68, s3
	v_ashrrev_i32_e32 v7, 31, v2
	s_add_i32 s62, s9, 0
	v_lshrrev_b32_e32 v7, 26, v7
	s_add_i32 s63, s62, 0x10000
	s_and_b32 s53, s2, 0xffff
	v_add_u32_e32 v7, v2, v7
	s_mov_b32 m0, s63
	s_add_i32 s69, s62, 0x12000
	v_lshlrev_b32_e32 v3, 5, v3
	v_lshlrev_b32_e32 v6, 3, v5
	v_lshrrev_b32_e32 v9, 6, v7
	v_and_b32_e32 v7, 0xc0, v7
	buffer_load_dwordx4 v199, s[52:55], 0 offen lds
	s_mov_b32 m0, s69
	s_add_i32 s70, s62, 0x14000
	v_and_b32_e32 v3, 32, v3
	v_ashrrev_i16_sdwa v1, v231, sext(v1) dst_sel:DWORD dst_unused:UNUSED_PAD src0_sel:DWORD src1_sel:BYTE_0
	v_and_b32_e32 v6, 0x1ffff0, v6
	v_lshlrev_b32_e32 v5, 5, v5
	v_sub_u32_e32 v2, v2, v7
	buffer_load_dwordx4 v228, s[52:55], 0 offen lds
	s_mov_b32 m0, s70
	s_add_i32 s71, s62, 0x16000
	v_bfe_i32 v1, v1, 0, 16
	v_add_u32_e32 v6, v9, v6
	v_and_b32_e32 v5, 32, v5
	v_ashrrev_i16_sdwa v2, v231, sext(v2) dst_sel:DWORD dst_unused:UNUSED_PAD src0_sel:DWORD src1_sel:BYTE_0
	v_lshl_or_b32 v3, v4, 10, v3
	buffer_load_dwordx4 v199, s[52:55], s89 offen lds
	s_mov_b32 m0, s71
	v_bfe_i32 v2, v2, 0, 16
	v_lshl_or_b32 v4, v6, 10, v5
	v_add_lshl_u32 v229, v3, v1, 1
	buffer_load_dwordx4 v228, s[52:55], s89 offen lds
	s_and_b32 s41, s13, 0xffff
	s_mov_b32 s42, s54
	s_mov_b32 s43, s55
	s_mov_b32 m0, s62
	s_add_i32 s72, s62, 0x2000
	v_add_lshl_u32 v252, v4, v2, 1
	buffer_load_dwordx4 v229, s[40:43], 0 offen lds
	s_mov_b32 m0, s72
	s_add_i32 s73, s62, 0x4000
	buffer_load_dwordx4 v252, s[40:43], 0 offen lds
	s_mov_b32 m0, s73
	s_add_i32 s74, s62, 0x6000
	buffer_load_dwordx4 v229, s[40:43], s89 offen lds
	s_mov_b32 m0, s74
	s_cmp_eq_u32 s12, 1
	buffer_load_dwordx4 v252, s[40:43], s89 offen lds
	s_cselect_b64 s[2:3], -1, 0
	s_add_u32 s8, s0, 0x58000000
	s_addc_u32 s9, s1, 0
	s_add_i32 s75, s62, 0x18000
	s_mov_b32 m0, s75
	s_movk_i32 s13, 0x80
	s_add_i32 s76, s62, 0x1a000
	buffer_load_dwordx4 v199, s[52:55], s13 offen lds
	s_mov_b32 m0, s76
	s_add_i32 s77, s62, 0x8000
	buffer_load_dwordx4 v228, s[52:55], s13 offen lds
	s_mov_b32 s42, s54
	s_mov_b32 s43, s55
	s_mov_b32 m0, s77
	s_add_i32 s80, s62, 0xa000
	buffer_load_dwordx4 v229, s[40:43], s13 offen lds
	s_mov_b32 m0, s80
	s_add_i32 s82, s62, 0x1c000
	buffer_load_dwordx4 v252, s[40:43], s13 offen lds
	s_mov_b32 m0, s82
	s_mov_b32 s13, 0x40080
	s_add_i32 s83, s62, 0x1e000
	buffer_load_dwordx4 v199, s[52:55], s13 offen lds
	s_mov_b32 m0, s83
	s_sext_i32_i8 s78, s4
	buffer_load_dwordx4 v228, s[52:55], s13 offen lds
	s_cmp_lg_u32 s12, 1
	s_cbranch_scc1 .LBB0_1493
	s_barrier
.LBB0_1493:
	s_waitcnt vmcnt(8)
	s_barrier
	s_and_b32 s4, s5, 3
	v_and_b32_e32 v1, 48, v0
	v_lshlrev_b32_e32 v2, 6, v0
	s_movk_i32 s13, 0x3c0
	v_lshlrev_b32_e32 v0, 2, v0
	s_lshl_b32 s88, s12, 6
	s_lshl_b32 s12, s12, 13
	v_and_or_b32 v1, v2, s13, v1
	v_and_b32_e32 v0, 32, v0
	s_lshl_b32 s89, s4, 5
	s_lshl_b32 s4, s4, 12
	s_waitcnt vmcnt(6)
	s_add_i32 s90, s62, 0xc000
	v_bitop3_b32 v2, v1, s12, v0 bitop3:0xde
	v_bitop3_b32 v0, v1, s4, v0 bitop3:0xde
	s_cmp_lt_u32 s5, 4
	v_mov_b32_e32 v9, v8
	v_mov_b32_e32 v10, v8
	v_mov_b32_e32 v11, v8
	s_cselect_b64 s[18:19], -1, 0
	s_ashr_i32 s91, s88, 31
	s_add_i32 s92, s62, 0xe000
	s_ashr_i32 s93, s33, 31
	s_mov_b32 s94, 0
	v_add_u32_e32 v176, 0, v0
	v_add_u32_e32 v198, 0, v2
	s_mov_b64 s[42:43], s[54:55]
	s_mov_b64 s[4:5], s[54:55]
	s_barrier
	s_branch .LBB0_1496

.LBB0_1522:
	s_andn2_b64 vcc, exec, s[2:3]
	s_cbranch_vccnz .LBB0_1562
	s_lshl_b32 s5, s8, 6
	v_add_u32_e32 v1, s5, v0
	v_ashrrev_i32_e32 v3, 31, v1
	v_lshrrev_b32_e32 v3, 26, v3
	v_lshlrev_b32_e32 v2, 4, v1
	v_add_u32_e32 v3, v1, v3
	v_bfe_i32 v1, v1, 27, 1
	v_lshrrev_b32_e32 v1, 22, v1
	v_add_u32_e32 v1, v2, v1
	v_and_b32_e32 v1, 0xfffffc00, v1
	v_sub_u32_e32 v1, v2, v1
	v_lshrrev_b32_e32 v4, 4, v1
	v_bitop3_b32 v1, v4, v1, 32 bitop3:0x6c
	v_ashrrev_i32_e32 v5, 31, v1
	v_ashrrev_i32_e32 v3, 6, v3
	v_lshrrev_b32_e32 v5, 26, v5
	v_lshlrev_b32_e32 v4, 3, v3
	v_add_u32_e32 v5, v1, v5
	v_and_b32_e32 v4, -16, v4
	v_ashrrev_i32_e32 v6, 6, v5
	v_and_b32_e32 v5, 0xc0, v5
	v_add_u32_e32 v4, v6, v4
	v_sub_u32_e32 v1, v1, v5
	v_lshlrev_b32_e32 v3, 5, v3
	v_ashrrev_i16_sdwa v1, v231, sext(v1) dst_sel:DWORD dst_unused:UNUSED_PAD src0_sel:DWORD src1_sel:BYTE_0
	v_lshlrev_b32_e32 v5, 1, v4
	v_lshrrev_b32_e32 v7, 2, v4
	v_and_b32_e32 v6, 3, v6
	s_mov_b32 s2, 0xfffe0
	v_and_b32_e32 v3, 32, v3
	v_bfe_i32 v1, v1, 0, 16
	v_and_b32_e32 v5, 24, v5
	v_and_b32_e32 v7, 4, v7
	v_and_or_b32 v4, v4, s2, v6
	v_or3_b32 v4, v4, v7, v5
	v_add_lshl_u32 v1, v3, v1, 1
	v_lshl_add_u32 v170, v4, 12, v1
	v_add_u32_e32 v1, 0x2000, v2
	v_ashrrev_i32_e32 v2, 31, v1
	v_lshrrev_b32_e32 v2, 22, v2
	v_add_u32_e32 v2, v1, v2
	v_ashrrev_i32_e32 v2, 10, v2
	v_mul_i32_i24_e32 v3, 0x400, v2
	v_sub_u32_e32 v1, v1, v3
	v_lshrrev_b32_e32 v3, 4, v1
	v_bitop3_b32 v1, v3, v1, 32 bitop3:0x6c
	v_ashrrev_i32_e32 v4, 31, v1
	v_lshrrev_b32_e32 v4, 26, v4
	v_lshlrev_b32_e32 v3, 3, v2
	v_add_u32_e32 v4, v1, v4
	v_and_b32_e32 v3, -16, v3
	v_ashrrev_i32_e32 v5, 6, v4
	v_and_b32_e32 v4, 0xc0, v4
	v_add_u32_e32 v3, v5, v3
	v_sub_u32_e32 v1, v1, v4
	v_lshlrev_b32_e32 v2, 5, v2
	v_ashrrev_i16_sdwa v1, v231, sext(v1) dst_sel:DWORD dst_unused:UNUSED_PAD src0_sel:DWORD src1_sel:BYTE_0
	v_lshlrev_b32_e32 v4, 1, v3
	v_lshrrev_b32_e32 v6, 2, v3
	v_and_b32_e32 v5, 3, v5
	v_and_b32_e32 v2, 32, v2
	v_bfe_i32 v1, v1, 0, 16
	v_and_b32_e32 v4, 24, v4
	v_and_b32_e32 v6, 4, v6
	v_and_or_b32 v3, v3, s2, v5
	v_or3_b32 v3, v3, v6, v4
	v_add_lshl_u32 v1, v2, v1, 1
	v_lshl_add_u32 v171, v3, 12, v1
	v_mov_b32 v48, 0
	v_mbcnt_lo_u32_b32 v1, -1, 0
	v_mbcnt_hi_u32_b32 v1, -1, v1
	s_ashr_i32 s63, s62, 31
	v_add_u32_e32 v1, s5, v1
	v_ashrrev_i32_e32 v3, 31, v1
	v_lshrrev_b32_e32 v3, 26, v3
	v_lshlrev_b32_e32 v2, 4, v1
	v_add_u32_e32 v3, v1, v3
	v_bfe_i32 v1, v1, 27, 1
	v_lshrrev_b32_e32 v1, 22, v1
	v_add_u32_e32 v1, v2, v1
	v_and_b32_e32 v1, 0xfffffc00, v1
	v_sub_u32_e32 v1, v2, v1
	v_lshrrev_b32_e32 v4, 4, v1
	v_bitop3_b32 v1, v4, v1, 32 bitop3:0x6c
	v_ashrrev_i32_e32 v5, 31, v1
	v_lshrrev_b32_e32 v5, 26, v5
	v_add_u32_e32 v5, v1, v5
	v_lshrrev_b32_e32 v6, 6, v5
	v_and_b32_e32 v5, 0xc0, v5
	v_add_u32_e32 v2, 0x2000, v2
	v_sub_u32_e32 v1, v1, v5
	v_ashrrev_i32_e32 v5, 31, v2
	v_ashrrev_i32_e32 v3, 6, v3
	v_lshrrev_b32_e32 v5, 22, v5
	v_lshlrev_b32_e32 v4, 3, v3
	v_add_u32_e32 v5, v2, v5
	s_ashr_i32 s4, s8, 2
	s_lshl_b32 s9, s8, 10
	s_lshl_b64 s[2:3], s[62:63], 20
	v_and_b32_e32 v4, 0xffff0, v4
	v_ashrrev_i32_e32 v5, 10, v5
	s_add_u32 s40, s65, s2
	v_add_u32_e32 v4, v6, v4
	v_mul_i32_i24_e32 v6, 0x400, v5
	s_addc_u32 s12, s66, s3
	s_ashr_i32 s59, s58, 31
	v_sub_u32_e32 v2, v2, v6
	s_lshl_b64 s[2:3], s[58:59], 20
	v_lshrrev_b32_e32 v6, 4, v2
	s_add_u32 s52, s67, s2
	v_bitop3_b32 v2, v6, v2, 32 bitop3:0x6c
	s_addc_u32 s2, s68, s3
	v_ashrrev_i32_e32 v7, 31, v2
	s_add_i32 s59, s9, 0
	v_lshrrev_b32_e32 v7, 26, v7
	s_add_i32 s61, s59, 0x10000
	s_and_b32 s53, s2, 0xffff
	v_add_u32_e32 v7, v2, v7
	s_mov_b32 m0, s61
	s_add_i32 s69, s59, 0x12000
	v_lshlrev_b32_e32 v3, 5, v3
	v_lshlrev_b32_e32 v6, 3, v5
	s_waitcnt vmcnt(0)
	v_lshrrev_b32_e32 v8, 6, v7
	v_and_b32_e32 v7, 0xc0, v7
	buffer_load_dwordx4 v170, s[52:55], 0 offen lds
	s_mov_b32 m0, s69
	s_add_i32 s70, s59, 0x14000
	v_and_b32_e32 v3, 32, v3
	v_ashrrev_i16_sdwa v1, v231, sext(v1) dst_sel:DWORD dst_unused:UNUSED_PAD src0_sel:DWORD src1_sel:BYTE_0
	v_and_b32_e32 v6, 0xffff0, v6
	v_lshlrev_b32_e32 v5, 5, v5
	v_sub_u32_e32 v2, v2, v7
	buffer_load_dwordx4 v171, s[52:55], 0 offen lds
	s_mov_b32 m0, s70
	s_add_i32 s71, s59, 0x16000
	v_bfe_i32 v1, v1, 0, 16
	v_add_u32_e32 v6, v8, v6
	v_and_b32_e32 v5, 32, v5
	v_ashrrev_i16_sdwa v2, v231, sext(v2) dst_sel:DWORD dst_unused:UNUSED_PAD src0_sel:DWORD src1_sel:BYTE_0
	v_lshl_or_b32 v3, v4, 11, v3
	buffer_load_dwordx4 v170, s[52:55], s95 offen lds
	s_mov_b32 m0, s71
	v_bfe_i32 v2, v2, 0, 16
	v_lshl_or_b32 v4, v6, 11, v5
	v_add_lshl_u32 v172, v3, v1, 1
	buffer_load_dwordx4 v171, s[52:55], s95 offen lds
	s_and_b32 s41, s12, 0xffff
	s_mov_b32 s42, s54
	s_mov_b32 s43, s55
	s_mov_b32 m0, s59
	s_add_i32 s72, s59, 0x2000
	v_add_lshl_u32 v173, v4, v2, 1
	buffer_load_dwordx4 v172, s[40:43], 0 offen lds
	s_mov_b32 m0, s72
	s_add_i32 s73, s59, 0x4000
	buffer_load_dwordx4 v173, s[40:43], 0 offen lds
	s_mov_b32 m0, s73
	s_add_i32 s74, s59, 0x6000
	buffer_load_dwordx4 v172, s[40:43], s95 offen lds
	s_mov_b32 m0, s74
	s_cmp_eq_u32 s4, 1
	buffer_load_dwordx4 v173, s[40:43], s95 offen lds
	s_cselect_b64 s[2:3], -1, 0
	s_add_u32 s0, s0, 0x800000
	s_addc_u32 s1, s1, 0
	s_add_i32 s75, s59, 0x18000
	s_mov_b32 m0, s75
	s_movk_i32 s5, 0x80
	s_add_i32 s76, s59, 0x1a000
	buffer_load_dwordx4 v170, s[52:55], s5 offen lds
	s_mov_b32 m0, s76
	s_add_i32 s77, s59, 0x8000
	buffer_load_dwordx4 v171, s[52:55], s5 offen lds
	s_mov_b32 s42, s54
	s_mov_b32 s43, s55
	s_mov_b32 m0, s77
	s_add_i32 s82, s59, 0xa000
	buffer_load_dwordx4 v172, s[40:43], s5 offen lds
	s_mov_b32 m0, s82
	s_add_i32 s83, s59, 0x1c000
	buffer_load_dwordx4 v173, s[40:43], s5 offen lds
	s_mov_b32 m0, s83
	s_mov_b32 s5, 0x80080
	s_add_i32 s88, s59, 0x1e000
	buffer_load_dwordx4 v170, s[52:55], s5 offen lds
	s_mov_b32 m0, s88
	v_and_b32_e32 v1, 48, v0
	buffer_load_dwordx4 v171, s[52:55], s5 offen lds
	s_cmp_lg_u32 s4, 1
	s_cbranch_scc1 .LBB0_1525
	s_barrier
.LBB0_1525:
	s_waitcnt vmcnt(8)
	s_barrier
	v_lshlrev_b32_e32 v2, 6, v0
	s_movk_i32 s5, 0x3c0
	v_lshlrev_b32_e32 v0, 2, v0
	s_and_b32 s89, s8, 3
	s_lshl_b32 s90, s4, 6
	s_lshl_b32 s4, s4, 13
	v_and_or_b32 v1, v2, s5, v1
	v_and_b32_e32 v0, 32, v0
	v_bitop3_b32 v2, v1, s4, v0 bitop3:0xde
	s_lshl_b32 s91, s89, 5
	s_lshl_b32 s4, s89, 12
	s_waitcnt vmcnt(6)
	s_add_i32 s92, s59, 0xc000
	v_bitop3_b32 v0, v1, s4, v0 bitop3:0xde
	s_cmp_lt_u32 s8, 4
	v_mov_b32_e32 v49, v48
	v_mov_b32_e32 v50, v48
	v_mov_b32_e32 v51, v48
	s_cselect_b64 s[8:9], -1, 0
	s_ashr_i32 s93, s90, 31
	s_add_i32 s94, s59, 0xe000
	s_ashr_i32 s95, s33, 31
	s_ashr_i32 s96, s64, 31
	s_mov_b32 s78, 0
	v_add_u32_e32 v174, 0, v0
	v_add_u32_e32 v175, 0, v2
	s_mov_b64 s[42:43], s[54:55]
	s_mov_b64 s[4:5], s[54:55]
	s_barrier
	s_branch .LBB0_1528

.LBB0_1812:
	s_or_b64 exec, exec, s[0:1]
	v_readlane_b32 s0, v255, 9
	s_mov_b32 s4, s91
	s_waitcnt lgkmcnt(0)
	s_waitcnt vmcnt(16) lgkmcnt(0)
	v_mov_b32_e32 v0, s0
	s_barrier
	v_mbcnt_lo_u32_b32 v4, -1, 0
	v_mbcnt_hi_u32_b32 v4, -1, v4
	ds_read_b32 v0, v0
	s_waitcnt lgkmcnt(0)
	v_readfirstlane_b32 s0, v0
	s_lshl_b32 s1, s0, 3
	s_cmp_ge_i32 s34, s1
	s_cbranch_scc1 .LBB0_1832
	s_add_u32 s35, s2, 0x22000000
	s_addc_u32 s56, s3, 0
	s_lshl_b32 s1, s4, 6
	v_add_u32_e32 v0, s1, v4
	v_ashrrev_i32_e32 v2, 31, v0
	v_lshrrev_b32_e32 v2, 26, v2
	v_lshlrev_b32_e32 v1, 4, v0
	v_add_u32_e32 v2, v0, v2
	v_bfe_i32 v0, v0, 27, 1
	v_lshrrev_b32_e32 v0, 22, v0
	v_add_u32_e32 v0, v1, v0
	v_and_b32_e32 v0, 0xfffffc00, v0
	v_sub_u32_e32 v0, v1, v0
	v_lshrrev_b32_e32 v3, 4, v0
	v_bitop3_b32 v0, v3, v0, 32 bitop3:0x6c
	v_ashrrev_i32_e32 v5, 31, v0
	v_lshrrev_b32_e32 v5, 26, v5
	v_ashrrev_i32_e32 v2, 6, v2
	v_add_u32_e32 v5, v0, v5
	v_lshlrev_b32_e32 v3, 3, v2
	v_ashrrev_i32_e32 v6, 6, v5
	v_and_b32_e32 v5, 0xc0, v5
	v_and_b32_e32 v3, -16, v3
	v_lshlrev_b32_e32 v2, 5, v2
	v_sub_u32_e32 v0, v0, v5
	s_ashr_i32 s5, s4, 2
	s_lshl_b32 s8, s4, 10
	v_add_u32_e32 v3, v6, v3
	v_and_b32_e32 v2, 32, v2
	v_ashrrev_i16_sdwa v0, v231, sext(v0) dst_sel:DWORD dst_unused:UNUSED_PAD src0_sel:DWORD src1_sel:BYTE_0
	s_add_u32 s57, s2, 0x31000000
	v_add_u32_sdwa v0, v2, sext(v0) dst_sel:DWORD dst_unused:UNUSED_PAD src0_sel:DWORD src1_sel:WORD_0
	v_lshlrev_b32_e32 v2, 1, v3
	v_lshrrev_b32_e32 v5, 2, v3
	v_and_b32_e32 v6, 3, v6
	s_mov_b32 s23, 0xffffe0
	s_addc_u32 s58, s3, 0
	s_ashr_i32 s59, s34, 31
	v_and_b32_e32 v2, 24, v2
	v_and_b32_e32 v5, 4, v5
	v_and_or_b32 v3, v3, s23, v6
	s_lshr_b32 s9, s59, 29
	v_or3_b32 v2, v3, v5, v2
	s_add_i32 s9, s34, s9
	v_mul_u32_u24_e32 v2, 0xb00, v2
	s_ashr_i32 s12, s9, 3
	s_and_b32 s9, s9, -8
	v_add_lshl_u32 v130, v0, v2, 1
	v_add_u32_e32 v0, 0x2000, v1
	s_sub_i32 s9, s34, s9
	v_ashrrev_i32_e32 v1, 31, v0
	s_lshr_b32 s13, s9, 31
	v_lshrrev_b32_e32 v1, 22, v1
	s_add_i32 s13, s0, s13
	v_add_u32_e32 v1, v0, v1
	s_mul_i32 s9, s13, s9
	v_ashrrev_i32_e32 v1, 10, v1
	s_add_i32 s9, s9, s12
	v_mul_i32_i24_e32 v2, 0x400, v1
	s_ashr_i32 s12, s9, 31
	v_sub_u32_e32 v0, v0, v2
	s_lshr_b32 s12, s12, 26
	v_lshrrev_b32_e32 v2, 4, v0
	s_add_i32 s12, s9, s12
	v_bitop3_b32 v0, v2, v0, 32 bitop3:0x6c
	s_ashr_i32 s13, s12, 6
	v_ashrrev_i32_e32 v3, 31, v0
	s_lshl_b32 s13, s13, 3
	v_lshrrev_b32_e32 v3, 26, v3
	s_sub_i32 s0, s0, s13
	v_add_u32_e32 v3, v0, v3
	s_min_i32 s0, s0, 8
	v_ashrrev_i32_e32 v5, 6, v3
	v_and_b32_e32 v3, 0xc0, v3
	s_abs_i32 s18, s0
	v_sub_u32_e32 v0, v0, v3
	v_cvt_f32_u32_e32 v3, s18
	s_sub_i32 s20, 0, s18
	s_andn2_b32 s12, s12, 63
	s_sub_i32 s9, s9, s12
	v_rcp_iflag_f32_e32 v3, v3
	s_abs_i32 s19, s9
	s_xor_b32 s12, s9, s0
	s_ashr_i32 s12, s12, 31
	v_mul_f32_e32 v3, 0x4f7ffffe, v3
	v_cvt_u32_f32_e32 v3, v3
	v_lshlrev_b32_e32 v2, 3, v1
	v_and_b32_e32 v2, -16, v2
	v_lshlrev_b32_e32 v1, 5, v1
	v_readfirstlane_b32 s21, v3
	s_mul_i32 s20, s20, s21
	s_mul_hi_u32 s20, s21, s20
	s_add_i32 s21, s21, s20
	s_mul_hi_u32 s20, s19, s21
	s_mul_i32 s21, s20, s18
	s_sub_i32 s19, s19, s21
	s_add_i32 s21, s20, 1
	s_sub_i32 s22, s19, s18
	s_cmp_ge_u32 s19, s18
	s_cselect_b32 s20, s21, s20
	s_cselect_b32 s19, s22, s19
	s_add_i32 s21, s20, 1
	s_cmp_ge_u32 s19, s18
	s_cselect_b32 s18, s21, s20
	s_xor_b32 s18, s18, s12
	s_sub_i32 s90, s18, s12
	s_mul_i32 s0, s90, s0
	s_sub_i32 s0, s9, s0
	s_add_i32 s30, s13, s0
	s_lshl_b32 s0, s30, 2
	s_add_i32 s0, s0, 0
	v_add_u32_e32 v2, v5, v2
	v_and_b32_e32 v1, 32, v1
	v_ashrrev_i16_sdwa v0, v231, sext(v0) dst_sel:DWORD dst_unused:UNUSED_PAD src0_sel:DWORD src1_sel:BYTE_0
	s_add_i32 s0, s0, 0x22580
	v_add_u32_sdwa v0, v1, sext(v0) dst_sel:DWORD dst_unused:UNUSED_PAD src0_sel:DWORD src1_sel:WORD_0
	v_lshlrev_b32_e32 v1, 1, v2
	v_lshrrev_b32_e32 v6, 2, v2
	v_and_b32_e32 v5, 3, v5
	v_mov_b32_e32 v3, s0
	v_and_b32_e32 v1, 24, v1
	v_and_b32_e32 v6, 4, v6
	ds_read_b32 v3, v3
	v_and_or_b32 v2, v2, s23, v5
	v_or3_b32 v1, v2, v6, v1
	v_mul_u32_u24_e32 v1, 0xb00, v1
	v_add_lshl_u32 v131, v0, v1, 1
	v_mov_b32 v0, 0
	v_mbcnt_lo_u32_b32 v1, -1, 0
	v_mbcnt_hi_u32_b32 v1, -1, v1
	s_waitcnt lgkmcnt(0)
	v_readfirstlane_b32 s0, v3
	v_add_u32_e32 v1, s1, v1
	v_ashrrev_i32_e32 v3, 31, v1
	v_lshrrev_b32_e32 v3, 26, v3
	v_lshlrev_b32_e32 v2, 4, v1
	v_add_u32_e32 v3, v1, v3
	v_bfe_i32 v1, v1, 27, 1
	v_lshrrev_b32_e32 v1, 22, v1
	v_add_u32_e32 v1, v2, v1
	v_and_b32_e32 v1, 0xfffffc00, v1
	v_sub_u32_e32 v1, v2, v1
	v_lshrrev_b32_e32 v5, 4, v1
	v_bitop3_b32 v1, v5, v1, 32 bitop3:0x6c
	v_ashrrev_i32_e32 v6, 31, v1
	v_lshrrev_b32_e32 v6, 26, v6
	v_add_u32_e32 v6, v1, v6
	v_lshrrev_b32_e32 v7, 6, v6
	v_and_b32_e32 v6, 0xc0, v6
	v_add_u32_e32 v2, 0x2000, v2
	v_sub_u32_e32 v1, v1, v6
	v_ashrrev_i32_e32 v6, 31, v2
	v_ashrrev_i32_e32 v3, 6, v3
	v_lshrrev_b32_e32 v6, 22, v6
	v_lshlrev_b32_e32 v5, 3, v3
	v_add_u32_e32 v6, v2, v6
	s_and_b32 s0, s0, 0xff
	s_mul_i32 s12, s30, 0x160000
	v_and_b32_e32 v5, 0xfffff0, v5
	v_ashrrev_i32_e32 v6, 10, v6
	s_mul_hi_i32 s9, s30, 0x160000
	s_add_u32 s40, s57, s12
	v_add_u32_e32 v5, v7, v5
	v_mul_i32_i24_e32 v7, 0x400, v6
	s_addc_u32 s9, s58, s9
	s_mul_i32 s0, s0, 0xb00000
	v_sub_u32_e32 v2, v2, v7
	s_add_u32 s0, s35, s0
	v_lshrrev_b32_e32 v7, 4, v2
	s_addc_u32 s12, s56, 0
	s_mul_i32 s18, s90, 0x160000
	v_bitop3_b32 v2, v7, v2, 32 bitop3:0x6c
	s_mul_hi_i32 s13, s90, 0x160000
	s_add_u32 s52, s0, s18
	s_waitcnt vmcnt(0)
	v_ashrrev_i32_e32 v8, 31, v2
	s_addc_u32 s0, s12, s13
	v_lshrrev_b32_e32 v8, 26, v8
	s_add_i32 s61, s8, 0
	v_lshlrev_b32_e32 v7, 3, v6
	v_add_u32_e32 v8, v2, v8
	s_add_i32 s62, s61, 0x10000
	s_and_b32 s53, s0, 0xffff
	v_and_b32_e32 v7, 0xfffff0, v7
	v_lshrrev_b32_e32 v9, 6, v8
	s_movk_i32 s0, 0xb00
	s_mov_b32 m0, s62
	s_add_i32 s63, s61, 0x12000
	v_lshlrev_b32_e32 v3, 5, v3
	v_add_u32_e32 v7, v9, v7
	v_and_b32_e32 v8, 0xc0, v8
	v_mul_lo_u32 v5, v5, s0
	buffer_load_dwordx4 v130, s[52:55], 0 offen lds
	s_mov_b32 m0, s63
	s_add_i32 s64, s61, 0x14000
	v_ashrrev_i16_sdwa v1, v231, sext(v1) dst_sel:DWORD dst_unused:UNUSED_PAD src0_sel:DWORD src1_sel:BYTE_0
	v_sub_u32_e32 v2, v2, v8
	v_and_or_b32 v3, v3, 32, v5
	v_mul_lo_u32 v5, v7, s0
	buffer_load_dwordx4 v131, s[52:55], 0 offen lds
	s_mov_b32 m0, s64
	s_mov_b32 s0, 0xb0000
	s_add_i32 s65, s61, 0x16000
	v_bfe_i32 v1, v1, 0, 16
	v_lshlrev_b32_e32 v6, 5, v6
	v_ashrrev_i16_sdwa v2, v231, sext(v2) dst_sel:DWORD dst_unused:UNUSED_PAD src0_sel:DWORD src1_sel:BYTE_0
	buffer_load_dwordx4 v130, s[52:55], s0 offen lds
	s_mov_b32 m0, s65
	v_bfe_i32 v2, v2, 0, 16
	v_and_or_b32 v5, v6, 32, v5
	v_add_lshl_u32 v132, v3, v1, 1
	buffer_load_dwordx4 v131, s[52:55], s0 offen lds
	s_and_b32 s41, s9, 0xffff
	s_mov_b32 s42, s54
	s_mov_b32 s43, s55
	s_mov_b32 m0, s61
	s_add_i32 s66, s61, 0x2000
	v_add_lshl_u32 v133, v5, v2, 1
	buffer_load_dwordx4 v132, s[40:43], 0 offen lds
	s_mov_b32 m0, s66
	s_add_i32 s67, s61, 0x4000
	buffer_load_dwordx4 v133, s[40:43], 0 offen lds
	s_mov_b32 m0, s67
	s_add_i32 s68, s61, 0x6000
	buffer_load_dwordx4 v132, s[40:43], s0 offen lds
	s_mov_b32 m0, s68
	s_cmp_eq_u32 s5, 1
	buffer_load_dwordx4 v133, s[40:43], s0 offen lds
	s_cselect_b64 s[0:1], -1, 0
	s_add_u32 s2, s2, 0x48600000
	s_addc_u32 s3, s3, 0
	s_add_i32 s69, s61, 0x18000
	s_mov_b32 m0, s69
	s_movk_i32 s8, 0x80
	s_add_i32 s70, s61, 0x1a000
	buffer_load_dwordx4 v130, s[52:55], s8 offen lds
	s_mov_b32 m0, s70
	s_add_i32 s71, s61, 0x8000
	buffer_load_dwordx4 v131, s[52:55], s8 offen lds
	s_mov_b32 s42, s54
	s_mov_b32 s43, s55
	s_mov_b32 m0, s71
	s_add_i32 s72, s61, 0xa000
	buffer_load_dwordx4 v132, s[40:43], s8 offen lds
	s_mov_b32 m0, s72
	s_add_i32 s73, s61, 0x1c000
	buffer_load_dwordx4 v133, s[40:43], s8 offen lds
	s_mov_b32 m0, s73
	s_mov_b32 s8, 0xb0080
	s_add_i32 s74, s61, 0x1e000
	buffer_load_dwordx4 v130, s[52:55], s8 offen lds
	s_mov_b32 m0, s74
	v_and_b32_e32 v5, 48, v4
	buffer_load_dwordx4 v131, s[52:55], s8 offen lds
	s_cmp_lg_u32 s5, 1
	s_cbranch_scc1 .LBB0_1815
	s_barrier
.LBB0_1815:
	s_waitcnt vmcnt(8)
	s_barrier
	v_lshlrev_b32_e32 v6, 6, v4
	s_movk_i32 s8, 0x3c0
	v_lshlrev_b32_e32 v4, 2, v4
	s_lshl_b32 s75, s5, 6
	s_lshl_b32 s5, s5, 13
	v_and_or_b32 v5, v6, s8, v5
	v_and_b32_e32 v4, 32, v4
	v_bitop3_b32 v6, v5, s5, v4 bitop3:0xde
	s_lshl_b32 s5, s4, 5
	s_and_b32 s76, s5, 0x60
	s_lshl_b32 s5, s76, 7
	s_waitcnt vmcnt(6)
	s_add_i32 s77, s61, 0xc000
	v_bitop3_b32 v4, v5, s5, v4 bitop3:0xde
	s_cmp_lt_u32 s4, 4
	v_mov_b32_e32 v1, v0
	v_mov_b32_e32 v2, v0
	v_mov_b32_e32 v3, v0
	s_cselect_b64 s[8:9], -1, 0
	s_ashr_i32 s78, s75, 31
	s_add_i32 s79, s61, 0xe000
	s_ashr_i32 s80, s33, 31
	s_mov_b32 s82, 0
	v_add_u32_e32 v134, 0, v4
	v_add_u32_e32 v135, 0, v6
	s_mov_b64 s[42:43], s[54:55]
	s_mov_b64 s[4:5], s[54:55]
	s_barrier
	s_branch .LBB0_1818

.LBB0_1936:
	v_readlane_b32 s0, v254, 43
	v_readlane_b32 s1, v254, 44
	s_andn2_b64 vcc, exec, s[0:1]
	s_cbranch_vccnz .LBB0_1961
	v_mbcnt_lo_u32_b32 v0, -1, 0
	v_mbcnt_hi_u32_b32 v0, -1, v0
	v_readlane_b32 s0, v254, 2
	v_add_u32_e32 v0, s79, v0
	v_readlane_b32 s1, v254, 3
	s_load_dword s33, s[0:1], 0x0
	s_mov_b32 s61, s96
	s_mov_b32 s0, 24
	s_waitcnt lgkmcnt(0)
	s_mov_b32 s13, s91
	s_cmpk_gt_i32 s61, 0xaff
	v_mbcnt_lo_u32_b32 v4, -1, 0
	v_mbcnt_hi_u32_b32 v4, -1, v4
	s_cbranch_scc1 .LBB0_1961
	s_ashr_i32 s1, s0, 31
	s_lshl_b64 s[0:1], s[0:1], 3
	s_add_u32 s0, s92, s0
	s_addc_u32 s1, s93, s1
	s_load_dwordx2 s[4:5], s[0:1], 0x0
	s_mov_b32 s0, 0xfffe0
	s_movk_i32 s2, 0x161
	s_mov_b32 s46, s54
	s_mov_b32 s47, s55
	s_waitcnt lgkmcnt(0)
	s_add_u32 s62, s4, 0x2d000000
	s_addc_u32 s63, s5, 0
	s_add_u32 s64, s4, 0x7e00000
	s_addc_u32 s65, s5, 0
	s_lshl_b32 s66, s13, 6
	v_add_u32_e32 v0, s66, v4
	v_ashrrev_i32_e32 v2, 31, v0
	v_bfe_i32 v3, v0, 27, 1
	v_lshrrev_b32_e32 v2, 26, v2
	v_lshlrev_b32_e32 v1, 4, v0
	v_add_u32_e32 v0, v0, v2
	v_lshrrev_b32_e32 v2, 22, v3
	v_add_u32_e32 v2, v1, v2
	v_and_b32_e32 v2, 0xfffffc00, v2
	v_sub_u32_e32 v2, v1, v2
	v_lshrrev_b32_e32 v3, 4, v2
	v_bitop3_b32 v2, v3, v2, 32 bitop3:0x6c
	v_ashrrev_i32_e32 v5, 31, v2
	v_ashrrev_i32_e32 v0, 6, v0
	v_lshrrev_b32_e32 v5, 26, v5
	v_lshlrev_b32_e32 v3, 3, v0
	v_add_u32_e32 v5, v2, v5
	v_and_b32_e32 v3, -16, v3
	v_ashrrev_i32_e32 v6, 6, v5
	v_and_b32_e32 v5, 0xc0, v5
	v_add_u32_e32 v3, v6, v3
	v_sub_u32_e32 v2, v2, v5
	v_lshlrev_b32_e32 v0, 5, v0
	v_ashrrev_i16_sdwa v2, v231, sext(v2) dst_sel:DWORD dst_unused:UNUSED_PAD src0_sel:DWORD src1_sel:BYTE_0
	v_lshlrev_b32_e32 v5, 1, v3
	v_lshrrev_b32_e32 v7, 2, v3
	v_and_b32_e32 v6, 3, v6
	v_and_b32_e32 v0, 32, v0
	v_bfe_i32 v2, v2, 0, 16
	v_and_b32_e32 v5, 24, v5
	v_and_b32_e32 v7, 4, v7
	v_and_or_b32 v3, v3, s0, v6
	v_or3_b32 v3, v3, v7, v5
	v_add_lshl_u32 v0, v0, v2, 1
	v_lshl_add_u32 v134, v3, 12, v0
	v_add_u32_e32 v0, 0x2000, v1
	v_ashrrev_i32_e32 v1, 31, v0
	v_lshrrev_b32_e32 v1, 22, v1
	v_add_u32_e32 v1, v0, v1
	v_ashrrev_i32_e32 v1, 10, v1
	v_mul_i32_i24_e32 v2, 0x400, v1
	v_sub_u32_e32 v0, v0, v2
	v_lshrrev_b32_e32 v2, 4, v0
	v_bitop3_b32 v0, v2, v0, 32 bitop3:0x6c
	v_ashrrev_i32_e32 v3, 31, v0
	v_lshrrev_b32_e32 v3, 26, v3
	v_lshlrev_b32_e32 v2, 3, v1
	v_add_u32_e32 v3, v0, v3
	v_and_b32_e32 v2, -16, v2
	v_ashrrev_i32_e32 v5, 6, v3
	v_and_b32_e32 v3, 0xc0, v3
	v_add_u32_e32 v2, v5, v2
	v_sub_u32_e32 v0, v0, v3
	v_lshlrev_b32_e32 v1, 5, v1
	v_ashrrev_i16_sdwa v0, v231, sext(v0) dst_sel:DWORD dst_unused:UNUSED_PAD src0_sel:DWORD src1_sel:BYTE_0
	v_lshlrev_b32_e32 v3, 1, v2
	v_lshrrev_b32_e32 v6, 2, v2
	v_and_b32_e32 v5, 3, v5
	s_ashr_i32 s67, s61, 31
	v_and_b32_e32 v1, 32, v1
	v_bfe_i32 v0, v0, 0, 16
	v_and_b32_e32 v3, 24, v3
	v_and_b32_e32 v6, 4, v6
	v_and_or_b32 v2, v2, s0, v5
	s_lshr_b32 s0, s67, 29
	v_or3_b32 v2, v2, v6, v3
	v_add_lshl_u32 v0, v1, v0, 1
	s_add_i32 s0, s61, s0
	v_lshl_add_u32 v135, v2, 12, v0
	s_ashr_i32 s1, s0, 3
	s_and_b32 s0, s0, -8
	v_mov_b32 v0, 0
	v_mbcnt_lo_u32_b32 v1, -1, 0
	v_mbcnt_hi_u32_b32 v1, -1, v1
	s_ashr_i32 s20, s13, 2
	s_lshl_b32 s8, s13, 10
	s_sub_i32 s0, s61, s0
	v_add_u32_e32 v1, s66, v1
	s_cmp_lt_i32 s0, 0
	v_ashrrev_i32_e32 v3, 31, v1
	s_cselect_b32 s2, s2, 0x160
	v_lshrrev_b32_e32 v3, 26, v3
	s_mul_i32 s0, s0, s2
	v_lshlrev_b32_e32 v2, 4, v1
	v_add_u32_e32 v3, v1, v3
	v_bfe_i32 v1, v1, 27, 1
	s_add_i32 s0, s0, s1
	v_lshrrev_b32_e32 v1, 22, v1
	s_mul_hi_i32 s1, s0, 0x2e8ba2e9
	v_add_u32_e32 v1, v2, v1
	s_lshr_b32 s2, s1, 31
	s_ashr_i32 s1, s1, 6
	v_and_b32_e32 v1, 0xfffffc00, v1
	s_add_i32 s1, s1, s2
	v_sub_u32_e32 v1, v2, v1
	s_mul_i32 s2, s1, 0x160
	v_lshrrev_b32_e32 v5, 4, v1
	s_sub_i32 s0, s0, s2
	v_bitop3_b32 v1, v5, v1, 32 bitop3:0x6c
	s_bfe_u32 s2, s0, 0x3001c
	v_ashrrev_i32_e32 v6, 31, v1
	s_add_i32 s2, s0, s2
	v_lshrrev_b32_e32 v6, 26, v6
	s_sext_i32_i16 s3, s2
	s_and_b32 s2, s2, 0xfff8
	v_add_u32_e32 v6, v1, v6
	s_sub_i32 s0, s0, s2
	v_lshrrev_b32_e32 v7, 6, v6
	v_and_b32_e32 v6, 0xc0, v6
	v_add_u32_e32 v2, 0x2000, v2
	s_lshl_b32 s1, s1, 3
	s_sext_i32_i16 s0, s0
	v_sub_u32_e32 v1, v1, v6
	v_ashrrev_i32_e32 v6, 31, v2
	s_add_i32 s0, s1, s0
	v_ashrrev_i32_e32 v3, 6, v3
	v_lshrrev_b32_e32 v6, 22, v6
	s_ashr_i32 s1, s0, 31
	v_lshlrev_b32_e32 v5, 3, v3
	v_add_u32_e32 v6, v2, v6
	s_lshr_b32 s12, s3, 3
	s_lshl_b64 s[2:3], s[0:1], 20
	v_and_b32_e32 v5, 0xffff0, v5
	v_ashrrev_i32_e32 v6, 10, v6
	s_add_u32 s44, s62, s2
	v_add_u32_e32 v5, v7, v5
	v_mul_i32_i24_e32 v7, 0x400, v6
	s_addc_u32 s1, s63, s3
	s_bfe_i64 s[2:3], s[12:13], 0x100000
	v_sub_u32_e32 v2, v2, v7
	s_lshl_b64 s[2:3], s[2:3], 20
	v_lshrrev_b32_e32 v7, 4, v2
	s_add_u32 s52, s64, s2
	v_bitop3_b32 v2, v7, v2, 32 bitop3:0x6c
	s_addc_u32 s2, s65, s3
	s_waitcnt vmcnt(0)
	v_ashrrev_i32_e32 v8, 31, v2
	s_add_i32 s68, s8, 0
	v_lshrrev_b32_e32 v8, 26, v8
	s_add_i32 s69, s68, 0x10000
	s_and_b32 s53, s2, 0xffff
	v_add_u32_e32 v8, v2, v8
	s_mov_b32 m0, s69
	s_add_i32 s70, s68, 0x12000
	v_lshlrev_b32_e32 v3, 5, v3
	v_lshlrev_b32_e32 v7, 3, v6
	v_lshrrev_b32_e32 v9, 6, v8
	v_and_b32_e32 v8, 0xc0, v8
	buffer_load_dwordx4 v134, s[52:55], 0 offen lds
	s_mov_b32 m0, s70
	s_add_i32 s71, s68, 0x14000
	v_and_b32_e32 v3, 32, v3
	v_ashrrev_i16_sdwa v1, v231, sext(v1) dst_sel:DWORD dst_unused:UNUSED_PAD src0_sel:DWORD src1_sel:BYTE_0
	v_and_b32_e32 v7, 0xffff0, v7
	v_lshlrev_b32_e32 v6, 5, v6
	v_sub_u32_e32 v2, v2, v8
	buffer_load_dwordx4 v135, s[52:55], 0 offen lds
	s_mov_b32 m0, s71
	s_add_i32 s72, s68, 0x16000
	v_bfe_i32 v1, v1, 0, 16
	v_add_u32_e32 v7, v9, v7
	v_and_b32_e32 v6, 32, v6
	v_ashrrev_i16_sdwa v2, v231, sext(v2) dst_sel:DWORD dst_unused:UNUSED_PAD src0_sel:DWORD src1_sel:BYTE_0
	v_lshl_or_b32 v3, v5, 11, v3
	buffer_load_dwordx4 v134, s[52:55], s95 offen lds
	s_mov_b32 m0, s72
	v_bfe_i32 v2, v2, 0, 16
	v_lshl_or_b32 v5, v7, 11, v6
	v_add_lshl_u32 v136, v3, v1, 1
	buffer_load_dwordx4 v135, s[52:55], s95 offen lds
	s_and_b32 s45, s1, 0xffff
	s_mov_b32 m0, s68
	s_add_i32 s73, s68, 0x2000
	v_add_lshl_u32 v137, v5, v2, 1
	buffer_load_dwordx4 v136, s[44:47], 0 offen lds
	s_mov_b32 m0, s73
	s_add_i32 s74, s68, 0x4000
	buffer_load_dwordx4 v137, s[44:47], 0 offen lds
	s_mov_b32 m0, s74
	s_add_i32 s75, s68, 0x6000
	buffer_load_dwordx4 v136, s[44:47], s95 offen lds
	s_mov_b32 m0, s75
	s_cmp_eq_u32 s20, 1
	buffer_load_dwordx4 v137, s[44:47], s95 offen lds
	s_cselect_b64 s[2:3], -1, 0
	s_add_u32 s8, s4, 0x31000000
	s_addc_u32 s9, s5, 0
	s_add_u32 s18, s4, 0x800000
	s_addc_u32 s19, s5, 0
	s_add_i32 s76, s68, 0x18000
	s_mov_b32 m0, s76
	s_movk_i32 s1, 0x80
	s_add_i32 s77, s68, 0x1a000
	buffer_load_dwordx4 v134, s[52:55], s1 offen lds
	s_mov_b32 m0, s77
	s_add_i32 s78, s68, 0x8000
	buffer_load_dwordx4 v135, s[52:55], s1 offen lds
	s_mov_b32 s46, s54
	s_mov_b32 s47, s55
	s_mov_b32 m0, s78
	s_add_i32 s79, s68, 0xa000
	buffer_load_dwordx4 v136, s[44:47], s1 offen lds
	s_mov_b32 m0, s79
	s_add_i32 s80, s68, 0x1c000
	buffer_load_dwordx4 v137, s[44:47], s1 offen lds
	s_mov_b32 m0, s80
	s_mov_b32 s1, 0x80080
	s_add_i32 s82, s68, 0x1e000
	buffer_load_dwordx4 v134, s[52:55], s1 offen lds
	s_mov_b32 m0, s82
	v_and_b32_e32 v5, 48, v4
	buffer_load_dwordx4 v135, s[52:55], s1 offen lds
	s_cmp_lg_u32 s20, 1
	s_cbranch_scc1 .LBB0_1940
	s_barrier
.LBB0_1940:
	s_waitcnt vmcnt(8)
	s_barrier
	s_sext_i32_i16 s1, s12
	v_lshlrev_b32_e32 v6, 6, v4
	s_movk_i32 s12, 0x3c0
	v_lshlrev_b32_e32 v4, 2, v4
	s_and_b32 s4, s13, 3
	s_lshl_b32 s5, s20, 13
	v_and_or_b32 v5, v6, s12, v5
	v_and_b32_e32 v4, 32, v4
	s_lshl_b32 s83, s20, 6
	v_bitop3_b32 v6, v5, s5, v4 bitop3:0xde
	s_lshl_b32 s5, s4, 12
	s_waitcnt vmcnt(6)
	s_add_i32 s88, s68, 0xc000
	v_bitop3_b32 v4, v5, s5, v4 bitop3:0xde
	s_cmp_lt_u32 s13, 4
	v_mov_b32_e32 v1, v0
	v_mov_b32_e32 v2, v0
	v_mov_b32_e32 v3, v0
	s_cselect_b64 s[20:21], -1, 0
	s_lshl_b32 s89, s4, 4
	s_add_i32 s90, s68, 0xe000
	s_ashr_i32 s91, s33, 31
	s_mov_b32 s92, 0
	s_mov_b64 s[4:5], -1
	v_add_u32_e32 v138, 0, v4
	v_add_u32_e32 v139, 0, v6
	s_mov_b64 s[46:47], s[54:55]
	s_mov_b64 s[12:13], s[54:55]
	s_barrier
	s_branch .LBB0_1943

.LBB0_2016:
	s_load_dwordx2 s[4:5], s[0:1], 0x0
	s_andn2_b64 vcc, exec, s[2:3]
	s_cbranch_vccnz .LBB0_2056
	s_waitcnt lgkmcnt(0)
	s_add_u32 s59, s4, 0x31000000
	s_addc_u32 s61, s5, 0
	s_add_u32 s62, s4, 0x17000000
	s_addc_u32 s63, s5, 0
	s_lshl_b32 s0, s12, 6
	v_add_u32_e32 v1, s0, v0
	v_ashrrev_i32_e32 v3, 31, v1
	v_lshrrev_b32_e32 v3, 26, v3
	v_lshlrev_b32_e32 v2, 4, v1
	v_add_u32_e32 v3, v1, v3
	v_bfe_i32 v1, v1, 27, 1
	v_lshrrev_b32_e32 v1, 22, v1
	v_add_u32_e32 v1, v2, v1
	v_and_b32_e32 v1, 0xfffffc00, v1
	v_sub_u32_e32 v1, v2, v1
	v_lshrrev_b32_e32 v4, 4, v1
	v_bitop3_b32 v1, v4, v1, 32 bitop3:0x6c
	v_ashrrev_i32_e32 v5, 31, v1
	v_lshrrev_b32_e32 v5, 26, v5
	v_ashrrev_i32_e32 v3, 6, v3
	v_add_u32_e32 v5, v1, v5
	v_lshlrev_b32_e32 v4, 3, v3
	v_ashrrev_i32_e32 v6, 6, v5
	v_and_b32_e32 v5, 0xc0, v5
	v_and_b32_e32 v4, -16, v4
	v_lshlrev_b32_e32 v3, 5, v3
	v_sub_u32_e32 v1, v1, v5
	v_add_u32_e32 v4, v6, v4
	v_and_b32_e32 v3, 32, v3
	v_ashrrev_i16_sdwa v1, v231, sext(v1) dst_sel:DWORD dst_unused:UNUSED_PAD src0_sel:DWORD src1_sel:BYTE_0
	v_add_u32_sdwa v1, v3, sext(v1) dst_sel:DWORD dst_unused:UNUSED_PAD src0_sel:DWORD src1_sel:WORD_0
	v_lshlrev_b32_e32 v3, 1, v4
	v_lshrrev_b32_e32 v5, 2, v4
	v_and_b32_e32 v6, 3, v6
	s_mov_b32 s1, 0x3ffffe0
	v_and_b32_e32 v3, 24, v3
	v_and_b32_e32 v5, 4, v5
	v_and_or_b32 v4, v4, s1, v6
	v_or3_b32 v3, v4, v5, v3
	s_movk_i32 s9, 0x1640
	v_mul_lo_u32 v3, v3, s9
	v_add_lshl_u32 v174, v1, v3, 1
	v_add_u32_e32 v1, 0x2000, v2
	v_ashrrev_i32_e32 v2, 31, v1
	v_lshrrev_b32_e32 v2, 22, v2
	v_add_u32_e32 v2, v1, v2
	v_ashrrev_i32_e32 v2, 10, v2
	v_mul_i32_i24_e32 v3, 0x400, v2
	v_sub_u32_e32 v1, v1, v3
	v_lshrrev_b32_e32 v3, 4, v1
	v_bitop3_b32 v1, v3, v1, 32 bitop3:0x6c
	v_ashrrev_i32_e32 v4, 31, v1
	v_lshrrev_b32_e32 v4, 26, v4
	v_add_u32_e32 v4, v1, v4
	v_lshlrev_b32_e32 v3, 3, v2
	v_ashrrev_i32_e32 v5, 6, v4
	v_and_b32_e32 v4, 0xc0, v4
	v_and_b32_e32 v3, -16, v3
	v_lshlrev_b32_e32 v2, 5, v2
	v_sub_u32_e32 v1, v1, v4
	v_add_u32_e32 v3, v5, v3
	v_and_b32_e32 v2, 32, v2
	v_ashrrev_i16_sdwa v1, v231, sext(v1) dst_sel:DWORD dst_unused:UNUSED_PAD src0_sel:DWORD src1_sel:BYTE_0
	v_add_u32_sdwa v1, v2, sext(v1) dst_sel:DWORD dst_unused:UNUSED_PAD src0_sel:DWORD src1_sel:WORD_0
	v_lshlrev_b32_e32 v2, 1, v3
	v_lshrrev_b32_e32 v4, 2, v3
	v_and_b32_e32 v5, 3, v5
	v_and_b32_e32 v2, 24, v2
	v_and_b32_e32 v4, 4, v4
	v_and_or_b32 v3, v3, s1, v5
	v_or3_b32 v2, v3, v4, v2
	v_mul_lo_u32 v2, v2, s9
	v_add_lshl_u32 v175, v1, v2, 1
	v_mov_b32 v48, 0
	v_mbcnt_lo_u32_b32 v1, -1, 0
	v_mbcnt_hi_u32_b32 v1, -1, v1
	s_ashr_i32 s13, s12, 2
	v_add_u32_e32 v1, s0, v1
	v_ashrrev_i32_e32 v3, 31, v1
	v_lshrrev_b32_e32 v3, 26, v3
	v_lshlrev_b32_e32 v2, 4, v1
	v_add_u32_e32 v3, v1, v3
	v_bfe_i32 v1, v1, 27, 1
	v_lshrrev_b32_e32 v1, 22, v1
	v_add_u32_e32 v1, v2, v1
	v_and_b32_e32 v1, 0xfffffc00, v1
	v_sub_u32_e32 v1, v2, v1
	v_lshrrev_b32_e32 v4, 4, v1
	v_bitop3_b32 v1, v4, v1, 32 bitop3:0x6c
	v_ashrrev_i32_e32 v5, 31, v1
	v_lshrrev_b32_e32 v5, 26, v5
	v_add_u32_e32 v5, v1, v5
	v_lshrrev_b32_e32 v6, 6, v5
	v_and_b32_e32 v5, 0xc0, v5
	v_add_u32_e32 v2, 0x2000, v2
	v_sub_u32_e32 v1, v1, v5
	v_ashrrev_i32_e32 v5, 31, v2
	v_ashrrev_i32_e32 v3, 6, v3
	v_lshrrev_b32_e32 v5, 22, v5
	v_lshlrev_b32_e32 v4, 3, v3
	v_add_u32_e32 v5, v2, v5
	v_and_b32_e32 v4, 0x3fffff0, v4
	v_ashrrev_i32_e32 v5, 10, v5
	s_lshl_b32 s1, s12, 10
	s_mul_i32 s3, s56, 0x2c8000
	v_add_u32_e32 v4, v6, v4
	v_mul_i32_i24_e32 v6, 0x400, v5
	s_mul_hi_i32 s2, s56, 0x2c8000
	s_add_u32 s44, s59, s3
	v_sub_u32_e32 v2, v2, v6
	s_addc_u32 s2, s61, s2
	s_mul_i32 s8, s80, 0x2c8000
	v_lshrrev_b32_e32 v6, 4, v2
	s_mul_hi_i32 s3, s80, 0x2c8000
	s_add_u32 s52, s62, s8
	v_bitop3_b32 v2, v6, v2, 32 bitop3:0x6c
	s_addc_u32 s3, s63, s3
	v_ashrrev_i32_e32 v7, 31, v2
	s_add_i32 s64, s1, 0
	v_lshrrev_b32_e32 v7, 26, v7
	s_add_i32 s65, s64, 0x10000
	s_and_b32 s53, s3, 0xffff
	v_lshlrev_b32_e32 v6, 3, v5
	v_add_u32_e32 v7, v2, v7
	s_mov_b32 m0, s65
	s_add_i32 s66, s64, 0x12000
	v_and_b32_e32 v6, 0x3fffff0, v6
	s_waitcnt vmcnt(0)
	v_lshrrev_b32_e32 v8, 6, v7
	v_and_b32_e32 v7, 0xc0, v7
	buffer_load_dwordx4 v174, s[52:55], 0 offen lds
	s_mov_b32 m0, s66
	s_add_i32 s67, s64, 0x14000
	v_lshlrev_b32_e32 v3, 5, v3
	v_ashrrev_i16_sdwa v1, v231, sext(v1) dst_sel:DWORD dst_unused:UNUSED_PAD src0_sel:DWORD src1_sel:BYTE_0
	v_add_u32_e32 v6, v8, v6
	v_sub_u32_e32 v2, v2, v7
	v_mul_lo_u32 v4, v4, s9
	buffer_load_dwordx4 v175, s[52:55], 0 offen lds
	s_mov_b32 m0, s67
	s_mov_b32 s0, 0x164000
	s_add_i32 s68, s64, 0x16000
	v_bfe_i32 v1, v1, 0, 16
	v_lshlrev_b32_e32 v5, 5, v5
	v_ashrrev_i16_sdwa v2, v231, sext(v2) dst_sel:DWORD dst_unused:UNUSED_PAD src0_sel:DWORD src1_sel:BYTE_0
	v_and_or_b32 v3, v3, 32, v4
	v_mul_lo_u32 v4, v6, s9
	buffer_load_dwordx4 v174, s[52:55], s0 offen lds
	s_mov_b32 m0, s68
	v_bfe_i32 v2, v2, 0, 16
	v_and_or_b32 v4, v5, 32, v4
	v_add_lshl_u32 v176, v3, v1, 1
	buffer_load_dwordx4 v175, s[52:55], s0 offen lds
	s_and_b32 s45, s2, 0xffff
	s_mov_b32 s46, s54
	s_mov_b32 s47, s55
	s_mov_b32 m0, s64
	s_add_i32 s69, s64, 0x2000
	v_add_lshl_u32 v198, v4, v2, 1
	buffer_load_dwordx4 v176, s[44:47], 0 offen lds
	s_mov_b32 m0, s69
	s_add_i32 s70, s64, 0x4000
	buffer_load_dwordx4 v198, s[44:47], 0 offen lds
	s_mov_b32 m0, s70
	s_add_i32 s71, s64, 0x6000
	buffer_load_dwordx4 v176, s[44:47], s0 offen lds
	s_mov_b32 m0, s71
	s_cmp_eq_u32 s13, 1
	buffer_load_dwordx4 v198, s[44:47], s0 offen lds
	s_cselect_b64 s[0:1], -1, 0
	s_add_u32 s2, s4, 0x2d000000
	s_addc_u32 s3, s5, 0
	s_add_u32 s8, s4, 0x600000
	s_addc_u32 s9, s5, 0
	s_add_u32 s18, s4, 0x58000000
	s_addc_u32 s19, s5, 0
	s_add_i32 s72, s64, 0x18000
	s_mov_b32 m0, s72
	s_movk_i32 s4, 0x80
	s_add_i32 s73, s64, 0x1a000
	buffer_load_dwordx4 v174, s[52:55], s4 offen lds
	s_mov_b32 m0, s73
	s_add_i32 s74, s64, 0x8000
	buffer_load_dwordx4 v175, s[52:55], s4 offen lds
	s_mov_b32 s46, s54
	s_mov_b32 s47, s55
	s_mov_b32 m0, s74
	s_add_i32 s75, s64, 0xa000
	buffer_load_dwordx4 v176, s[44:47], s4 offen lds
	s_mov_b32 m0, s75
	s_add_i32 s76, s64, 0x1c000
	buffer_load_dwordx4 v198, s[44:47], s4 offen lds
	s_mov_b32 m0, s76
	s_mov_b32 s4, 0x164080
	s_add_i32 s77, s64, 0x1e000
	buffer_load_dwordx4 v174, s[52:55], s4 offen lds
	s_mov_b32 m0, s77
	v_and_b32_e32 v1, 48, v0
	buffer_load_dwordx4 v175, s[52:55], s4 offen lds
	s_cmp_lg_u32 s13, 1
	s_cbranch_scc1 .LBB0_2019
	s_barrier
.LBB0_2019:
	s_waitcnt vmcnt(8)
	s_barrier
	v_lshlrev_b32_e32 v2, 6, v0
	s_movk_i32 s5, 0x3c0
	v_lshlrev_b32_e32 v0, 2, v0
	s_and_b32 s78, s12, 3
	s_lshl_b32 s4, s13, 13
	v_and_or_b32 v1, v2, s5, v1
	v_and_b32_e32 v0, 32, v0
	s_lshl_b32 s79, s13, 6
	v_bitop3_b32 v2, v1, s4, v0 bitop3:0xde
	s_lshl_b32 s82, s78, 5
	s_lshl_b32 s4, s78, 12
	s_waitcnt vmcnt(6)
	s_add_i32 s83, s64, 0xc000
	v_bitop3_b32 v0, v1, s4, v0 bitop3:0xde
	s_cmp_lt_u32 s12, 4
	v_mov_b32_e32 v49, v48
	v_mov_b32_e32 v50, v48
	v_mov_b32_e32 v51, v48
	s_cselect_b64 s[20:21], -1, 0
	s_ashr_i32 s88, s79, 31
	s_add_i32 s89, s64, 0xe000
	s_ashr_i32 s90, s33, 31
	s_ashr_i32 s91, s58, 31
	s_mov_b32 s92, 0
	v_add_u32_e32 v199, 0, v0
	v_add_u32_e32 v200, 0, v2
	s_mov_b64 s[46:47], s[54:55]
	s_mov_b64 s[4:5], s[54:55]
	s_barrier
	s_branch .LBB0_2022
